# speedup vs baseline: 1.0098x; 1.0034x over previous
.LBB2_9:
	s_or_b64 exec, exec, s[12:13]
	v_bfe_u32 v58, v0, 4, 2
	v_and_b32_e32 v74, 15, v0
	v_lshlrev_b32_e32 v71, 4, v58
	s_movk_i32 s12, 0x110
	v_mad_u32_u24 v70, v74, s12, v71
	ds_read_b128 v[76:79], v70
	ds_read_b128 v[80:83], v70 offset:64
	ds_read_b128 v[84:87], v70 offset:4352
	ds_read_b128 v[88:91], v70 offset:4416
	s_waitcnt vmcnt(6) lgkmcnt(0)
	v_mfma_f32_16x16x32_f16 v[76:79], v[14:17], v[76:79], v[18:21]
	v_and_b32_e32 v57, 0x70, v57
	v_lshlrev_b32_e32 v57, 1, v57
	v_lshlrev_b32_e32 v58, 3, v58
	v_mfma_f32_16x16x32_f16 v[84:87], v[14:17], v[84:87], v[18:21]
	s_movk_i32 s13, 0x4400
	v_or3_b32 v72, v57, v58, s13
	v_mad_u32_u24 v57, v74, s12, v72
	v_mfma_f32_16x16x32_f16 v[76:79], v[10:13], v[80:83], v[76:79]
	ds_read_b128 v[80:83], v70 offset:128
	ds_read_b128 v[92:95], v70 offset:192
	s_waitcnt lgkmcnt(1)
	v_mfma_f32_16x16x32_f16 v[76:79], v[6:9], v[80:83], v[76:79]
	v_mfma_f32_16x16x32_f16 v[80:83], v[10:13], v[88:91], v[84:87]
	s_nop 2
	ds_read_b128 v[84:87], v70 offset:4480
	ds_read_b128 v[88:91], v70 offset:4544
	s_waitcnt lgkmcnt(1)
	v_mfma_f32_16x16x32_f16 v[80:83], v[6:9], v[84:87], v[80:83]
	s_waitcnt lgkmcnt(0)
	v_mfma_f32_16x16x32_f16 v[80:83], v[2:5], v[88:91], v[80:83]
	ds_read_b128 v[84:87], v70 offset:8704
	ds_read_b128 v[88:91], v70 offset:8768
	s_waitcnt lgkmcnt(1)
	v_mfma_f32_16x16x32_f16 v[84:87], v[14:17], v[84:87], v[18:21]
	v_mfma_f32_16x16x32_f16 v[76:79], v[2:5], v[92:95], v[76:79]
	ds_read_b128 v[92:95], v70 offset:8832
	s_waitcnt lgkmcnt(1)
	v_mfma_f32_16x16x32_f16 v[84:87], v[10:13], v[88:91], v[84:87]
	ds_read_b128 v[88:91], v70 offset:8896
	s_nop 3
	v_cvt_pk_f16_f32 v59, v78, v79
	v_cvt_pk_f16_f32 v58, v76, v77
	s_waitcnt lgkmcnt(1)
	v_mfma_f32_16x16x32_f16 v[84:87], v[6:9], v[92:95], v[84:87]
	ds_read_b128 v[92:95], v70 offset:13056
	ds_read_b128 v[76:79], v70 offset:13120
	ds_write_b64 v57, v[58:59]
	s_waitcnt lgkmcnt(3)
	v_mfma_f32_16x16x32_f16 v[84:87], v[2:5], v[88:91], v[84:87]
	v_cvt_pk_f16_f32 v59, v82, v83
	v_cvt_pk_f16_f32 v58, v80, v81
	ds_read_b128 v[80:83], v70 offset:13248
	s_waitcnt lgkmcnt(3)
	v_mfma_f32_16x16x32_f16 v[88:91], v[14:17], v[92:95], v[18:21]
	ds_read_b128 v[92:95], v70 offset:13184
	ds_write_b64 v57, v[58:59] offset:4352
	s_nop 0
	v_cvt_pk_f16_f32 v59, v86, v87
	s_waitcnt lgkmcnt(4)
	v_mfma_f32_16x16x32_f16 v[76:79], v[10:13], v[76:79], v[88:91]
	v_cvt_pk_f16_f32 v58, v84, v85
	ds_write_b64 v57, v[58:59] offset:8704
	v_or_b32_e32 v70, 0x4400, v56
	s_waitcnt lgkmcnt(2)
	v_mfma_f32_16x16x32_f16 v[76:79], v[6:9], v[92:95], v[76:79]
	v_mfma_f32_16x16x32_f16 v[76:79], v[2:5], v[80:83], v[76:79]
	s_nop 7
	v_cvt_pk_f16_f32 v59, v78, v79
	v_cvt_pk_f16_f32 v58, v76, v77
	ds_write_b64 v57, v[58:59] offset:13056
	v_mov_b32_e32 v57, 0
	v_lshl_add_u64 v[58:59], s[10:11], 0, v[56:57]
	s_waitcnt lgkmcnt(0)
	s_barrier
	s_and_saveexec_b64 s[10:11], vcc
	s_cbranch_execz .LBB2_11
	v_mad_u32_u24 v57, v65, s12, v70
	ds_read_b128 v[76:79], v57
	v_lshlrev_b64 v[60:61], 8, v[60:61]
	v_lshl_add_u64 v[60:61], v[58:59], 0, v[60:61]
	s_waitcnt lgkmcnt(0)
	global_store_dwordx4 v[60:61], v[76:79], off

.LBB2_13:
	s_or_b64 exec, exec, s[10:11]
	v_mul_u32_u24_e32 v57, 0x110, v74
	s_andn2_b64 vcc, exec, s[8:9]
	v_add_u32_e32 v61, v73, v60
	v_add_u32_e32 v62, v73, v67
	v_add_u32_e32 v60, v73, v68
	s_cbranch_vccnz .LBB2_23
	s_waitcnt vmcnt(4)
	v_cvt_pk_f16_f32 v49, v48, v49
	v_cvt_pk_f16_f32 v48, v46, v47
	v_cvt_pk_f16_f32 v41, v40, v41
	v_cvt_pk_f16_f32 v40, v38, v39
	v_cvt_pk_f16_f32 v39, v52, v53
	v_cvt_pk_f16_f32 v38, v50, v51
	ds_write_b64 v61, v[48:49]
	ds_write_b64 v62, v[40:41]
	ds_write_b64 v61, v[38:39] offset:8704
	v_cvt_pk_f16_f32 v39, v44, v45
	v_cvt_pk_f16_f32 v38, v42, v43
	s_lshl_b32 s8, s14, 6
	ds_write_b64 v60, v[38:39]
	v_or_b32_e32 v38, s8, v65
	s_mov_b32 s9, 0xc350
	v_cmp_gt_i32_e32 vcc, s9, v38
	v_ashrrev_i32_e32 v39, 31, v38
	s_waitcnt lgkmcnt(0)
	s_barrier
	s_and_saveexec_b64 s[4:5], vcc
	s_cbranch_execz .LBB2_16
	s_movk_i32 s10, 0x110
	v_mad_u32_u24 v40, v65, s10, v56
	ds_read_b128 v[40:43], v40
	v_lshlrev_b64 v[44:45], 8, v[38:39]
	v_lshl_add_u64 v[44:45], v[54:55], 0, v[44:45]
	s_waitcnt lgkmcnt(0)
	global_store_dwordx4 v[44:45], v[40:43], off
